# read-once f32 loads non-temporal: P0 weight/x streams and the GEMM3 epilogue residual rows; no arithmetic change
# speedup vs baseline: 1.0330x; 1.0025x over previous
; __device__ __forceinline__ unsigned cvt_pk_bf16(float lo, float hi) { unsigned r; asm volatile("v_cvt_pk_bf16_f32 %0, %1, %2" : "=v"(r) : "v"(lo), "v"(hi)); return r; }
; __device__ __forceinline__ unsigned q8x4(const f32x4 a, const f32x4 g, float s) {
;     unsigned y[4];
; #pragma unroll
;     for (int i = 0; i < 4; ++i) y[i] = __float_as_uint(__builtin_fmaf(__builtin_amdgcn_fmed3f(a[i] * g[i] * s, -127.0f, 127.0f), 1.0f, 12582912.0f));
;     return __builtin_amdgcn_perm(y[1], y[0], 0x0c0c0400u) | __builtin_amdgcn_perm(y[3], y[2], 0x04000c0cu);
; }
;     __device__ __forceinline__ void operator()(const f32x4 (&acc)[2][2][4][2], const Unit& u, int wr, int wc, int fr, int fq) const {
;     ...
;         f32x4 gv[2][2];
; #pragma unroll
;         for (int bj = 0; bj < 2; ++bj)
; #pragma unroll
;             for (int n = 0; n < 2; ++n) gv[bj][n] = *(const f32x4*)(gain + col0 + bj * HALF + 4 * n);
;         float* SSQP = (float*)(ws + OFF_SSQP); unsigned char* Q8 = ws + OFF_Q8;
; #pragma unroll
;         for (int ai = 0; ai < 2; ++ai)
; #pragma unroll
;             for (int m = 0; m < 4; ++m) { const size_t r = (size_t)(row0 + ai * HALF + m * 16); float ss = 0.f;
; #pragma unroll
;                 for (int bj = 0; bj < 2; ++bj) { const size_t off = r * 4096 + col0 + bj * HALF;
;                     const f32x4 v0 = acc[ai][bj][m][0] * scale + *(const f32x4*)(R + off), v1 = acc[ai][bj][m][1] * scale + *(const f32x4*)(R + off + 4);
;                     ss += (v0[0] * v0[0] + v0[1] * v0[1]) + (v0[2] * v0[2] + v0[3] * v0[3]) + (v1[0] * v1[0] + v1[1] * v1[1]) + (v1[2] * v1[2] + v1[3] * v1[3]);
;                     u32x4 w; w.x = cvt_pk_bf16(v0[0], v0[1]); w.y = cvt_pk_bf16(v0[2], v0[3]); w.z = cvt_pk_bf16(v1[0], v1[1]); w.w = cvt_pk_bf16(v1[2], v1[3]);
;                     *(u32x4*)(HB + off) = w;
;                     u32x2e q; q.x = q8x4(v0, gv[bj][0], (float)HQS); q.y = q8x4(v1, gv[bj][1], (float)HQS);
;                     *(u32x2e*)(Q8 + r * LDQ8 + col0 + bj * HALF) = q; }
;                 ss += __shfl_xor(ss, 16); ss += __shfl_xor(ss, 32);
;                 if (fq == 0) SSQP[r * 64 + u.pn * 4 + wc] = ss; }
.LBB0_617:
	v_lshl_add_u32 v140, s29, 8, v169
	v_lshl_or_b32 v138, s28, 8, v170
	v_ashrrev_i32_e32 v141, 31, v140
	v_ashrrev_i32_e32 v139, 31, v138
	v_lshlrev_b64 v[66:67], 12, v[140:141]
	v_lshl_add_u64 v[154:155], v[66:67], 0, v[138:139]
	v_lshl_add_u64 v[156:157], v[154:155], 2, s[8:9]
	global_load_dwordx4 v[146:149], v[156:157], off nt
	global_load_dwordx4 v[150:153], v[156:157], off offset:16 nt
	v_lshl_add_u64 v[144:145], v[138:139], 2, s[52:53]
	global_load_dwordx4 v[74:77], v[144:145], off
	global_load_dwordx4 v[66:69], v[144:145], off offset:16
	v_cvt_f32_i32_e32 v159, v63
	v_cvt_f32_i32_e32 v158, v62
	v_cvt_f32_i32_e32 v161, v65
	v_cvt_f32_i32_e32 v160, v64
	v_cvt_f32_i32_e32 v179, v51
	v_cvt_f32_i32_e32 v178, v50
	v_cvt_f32_i32_e32 v181, v53
	v_cvt_f32_i32_e32 v180, v52
	v_lshlrev_b64 v[154:155], 1, v[154:155]
	global_load_dwordx4 v[50:53], v[144:145], off offset:528
	global_load_dwordx4 v[62:65], v[144:145], off offset:512
	v_lshl_add_u64 v[182:183], s[14:15], 0, v[154:155]
	v_readlane_b32 s22, v255, 13
	v_readlane_b32 s23, v255, 14
	v_cvt_f32_i32_e32 v135, v135
	v_cvt_f32_i32_e32 v134, v134
	v_lshl_add_u64 v[142:143], s[22:23], 0, v[138:139]
	v_mad_i64_i32 v[144:145], s[22:23], v140, s50, v[142:143]
	v_cvt_f32_i32_e32 v137, v137
	v_cvt_f32_i32_e32 v136, v136
	v_cvt_f32_i32_e32 v131, v131
	v_cvt_f32_i32_e32 v130, v130
	v_or_b32_e32 v154, 0x100, v154
	v_lshl_add_u64 v[154:155], s[14:15], 0, v[154:155]
	s_lshl_b32 s22, s28, 2
	s_ashr_i32 s23, s22, 31
	s_lshl_b64 s[22:23], s[22:23], 2
	s_add_u32 s22, s48, s22
	s_addc_u32 s23, s49, s23
	s_waitcnt vmcnt(5)
	v_pk_fma_f32 v[160:161], v[160:161], s[26:27], v[148:149] op_sel_hi:[1,0,1]
	v_pk_fma_f32 v[158:159], v[158:159], s[26:27], v[146:147] op_sel_hi:[1,0,1]
	s_waitcnt vmcnt(4)
	v_pk_fma_f32 v[180:181], v[180:181], s[26:27], v[152:153] op_sel_hi:[1,0,1]
	v_pk_fma_f32 v[178:179], v[178:179], s[26:27], v[150:151] op_sel_hi:[1,0,1]
	v_cvt_pk_bf16_f32 v146, v158, v159
	v_cvt_pk_bf16_f32 v147, v160, v161
	s_waitcnt vmcnt(3)
	v_mul_f32_e32 v150, v74, v158
	v_cvt_pk_bf16_f32 v148, v178, v179
	v_cvt_pk_bf16_f32 v149, v180, v181
	v_mul_f32_e32 v151, v75, v159
	v_mul_f32_e32 v152, v76, v160
	v_mul_f32_e32 v153, v77, v161
	s_waitcnt vmcnt(2)
	v_mul_f32_e32 v184, v66, v178
	v_mul_f32_e32 v185, v67, v179
	v_mul_f32_e32 v186, v68, v180
	v_mul_f32_e32 v187, v69, v181
	global_store_dwordx4 v[182:183], v[146:149], off
	v_mul_f32_e32 v159, v159, v159
	v_mul_f32_e32 v161, v161, v161
	v_mul_f32_e32 v146, 0x41c00000, v150
	v_mul_f32_e32 v147, 0x41c00000, v151
	v_mul_f32_e32 v148, 0x41c00000, v152
	v_mul_f32_e32 v149, 0x41c00000, v153
	v_mul_f32_e32 v150, 0x41c00000, v184
	v_mul_f32_e32 v151, 0x41c00000, v185
	v_mul_f32_e32 v152, 0x41c00000, v186
	v_mul_f32_e32 v153, 0x41c00000, v187
	v_med3_f32 v146, v146, s51, v177
	v_med3_f32 v147, v147, s51, v177
	v_med3_f32 v148, v148, s51, v177
	v_med3_f32 v149, v149, s51, v177
	v_med3_f32 v150, v150, s51, v177
	v_med3_f32 v151, v151, s51, v177
	v_med3_f32 v152, v152, s51, v177
	v_med3_f32 v153, v153, s51, v177
	v_add_f32_e32 v146, 0x4b400000, v146
	v_add_f32_e32 v147, 0x4b400000, v147
	v_add_f32_e32 v148, 0x4b400000, v148
	v_add_f32_e32 v149, 0x4b400000, v149
	v_add_f32_e32 v150, 0x4b400000, v150
	v_add_f32_e32 v151, 0x4b400000, v151
	v_add_f32_e32 v152, 0x4b400000, v152
	v_add_f32_e32 v153, 0x4b400000, v153
	v_perm_b32 v146, v147, v146, s56
	v_perm_b32 v147, v149, v148, s57
	v_perm_b32 v148, v151, v150, s56
	v_perm_b32 v149, v153, v152, s57
	v_or_b32_e32 v146, v146, v147
	v_or_b32_e32 v147, v148, v149
	global_store_dwordx2 v[144:145], v[146:147], off
	global_load_dwordx4 v[146:149], v[156:157], off offset:512 nt
	s_nop 0
	global_load_dwordx4 v[150:153], v[156:157], off offset:528 nt
	v_cvt_f32_i32_e32 v157, v133
	v_cvt_f32_i32_e32 v156, v132
	v_and_b32_e32 v133, 64, v176
	v_mul_f32_e32 v179, v179, v179
	v_fmac_f32_e32 v159, v158, v158
	v_fmac_f32_e32 v161, v160, v160
	v_xor_b32_e32 v132, 16, v176
	v_add_u32_e32 v133, 64, v133
	v_mul_f32_e32 v181, v181, v181
	v_fmac_f32_e32 v179, v178, v178
	v_add_f32_e32 v158, v159, v161
	v_cmp_lt_i32_e32 vcc, v132, v133
	v_fmac_f32_e32 v181, v180, v180
	v_add_f32_e32 v158, v158, v179
	v_cndmask_b32_e32 v132, v176, v132, vcc
	v_add_f32_e32 v158, v181, v158
	v_lshlrev_b32_e32 v132, 2, v132
	v_xor_b32_e32 v182, 32, v176
	v_cmp_lt_i32_e32 vcc, v182, v133
	s_waitcnt vmcnt(1)
	v_pk_fma_f32 v[148:149], v[136:137], s[26:27], v[148:149] op_sel_hi:[1,0,1]
	v_pk_fma_f32 v[146:147], v[134:135], s[26:27], v[146:147] op_sel_hi:[1,0,1]
	s_waitcnt vmcnt(0)
	v_pk_fma_f32 v[130:131], v[130:131], s[26:27], v[150:151] op_sel_hi:[1,0,1]
	v_mul_f32_e32 v150, v147, v147
	v_mul_f32_e32 v151, v149, v149
	v_pk_fma_f32 v[152:153], v[156:157], s[26:27], v[152:153] op_sel_hi:[1,0,1]
	v_mul_f32_e32 v156, v131, v131
	v_cvt_pk_bf16_f32 v134, v146, v147
	v_cvt_pk_bf16_f32 v135, v148, v149
	v_cvt_pk_bf16_f32 v136, v130, v131
	v_mul_f32_e32 v131, v51, v131
	v_fmac_f32_e32 v150, v146, v146
	v_fmac_f32_e32 v151, v148, v148
	v_mul_f32_e32 v157, v153, v153
	v_mul_f32_e32 v160, v64, v148
	v_fmac_f32_e32 v156, v130, v130
	v_mul_f32_e32 v131, 0x41c00000, v131
	v_add_f32_e32 v148, v150, v151
	v_mul_f32_e32 v149, v65, v149
	v_fmac_f32_e32 v157, v152, v152
	v_med3_f32 v131, v131, s51, v177
	v_add_f32_e32 v148, v148, v156
	v_cvt_pk_bf16_f32 v137, v152, v153
	global_store_dwordx4 v[154:155], v[134:137], off
	v_mul_f32_e32 v159, v62, v146
	v_mul_f32_e32 v147, v63, v147
	v_mul_f32_e32 v136, 0x41c00000, v149
	v_add_f32_e32 v149, 0x4b400000, v131
	v_add_f32_e32 v131, v157, v148
	v_add_f32_e32 v131, v158, v131
	ds_bpermute_b32 v148, v132, v131
	v_mul_f32_e32 v161, v50, v130
	v_mul_f32_e32 v130, 0x41c00000, v159
	v_mul_f32_e32 v134, 0x41c00000, v147
	v_mul_f32_e32 v135, 0x41c00000, v160
	v_med3_f32 v130, v130, s51, v177
	v_med3_f32 v134, v134, s51, v177
	v_med3_f32 v135, v135, s51, v177
	v_med3_f32 v136, v136, s51, v177
	v_add_f32_e32 v130, 0x4b400000, v130
	v_add_f32_e32 v134, 0x4b400000, v134
	v_add_f32_e32 v135, 0x4b400000, v135
	v_add_f32_e32 v136, 0x4b400000, v136
	v_cndmask_b32_e32 v133, v176, v182, vcc
	v_perm_b32 v130, v134, v130, s56
	v_perm_b32 v134, v136, v135, s57
	v_mul_f32_e32 v178, v52, v152
	v_mul_f32_e32 v153, v53, v153
	v_or_b32_e32 v134, v130, v134
	s_waitcnt lgkmcnt(0)
	v_add_f32_e32 v130, v131, v148
	v_lshlrev_b32_e32 v133, 2, v133
	v_mul_f32_e32 v137, 0x41c00000, v161
	v_mul_f32_e32 v146, 0x41c00000, v178
	v_mul_f32_e32 v147, 0x41c00000, v153
	ds_bpermute_b32 v131, v133, v130
	v_med3_f32 v137, v137, s51, v177
	v_med3_f32 v146, v146, s51, v177
	v_med3_f32 v147, v147, s51, v177
	v_add_f32_e32 v137, 0x4b400000, v137
	v_add_f32_e32 v146, 0x4b400000, v146
	v_add_f32_e32 v147, 0x4b400000, v147
	v_perm_b32 v135, v149, v137, s56
	v_perm_b32 v136, v147, v146, s57
	v_or_b32_e32 v135, v135, v136
	global_store_dwordx2 v[144:145], v[134:135], off offset:128
	s_and_saveexec_b64 s[28:29], s[0:1]
	s_cbranch_execz .LBB0_619
; __device__ __forceinline__ unsigned cvt_pk_bf16(float lo, float hi) { unsigned r; asm volatile("v_cvt_pk_bf16_f32 %0, %1, %2" : "=v"(r) : "v"(lo), "v"(hi)); return r; }
; __device__ __forceinline__ unsigned q8x4(const f32x4 a, const f32x4 g, float s) {
;     unsigned y[4];
; #pragma unroll
;     for (int i = 0; i < 4; ++i) y[i] = __float_as_uint(__builtin_fmaf(__builtin_amdgcn_fmed3f(a[i] * g[i] * s, -127.0f, 127.0f), 1.0f, 12582912.0f));
;     return __builtin_amdgcn_perm(y[1], y[0], 0x0c0c0400u) | __builtin_amdgcn_perm(y[3], y[2], 0x04000c0cu);
; }
;     __device__ __forceinline__ void operator()(const f32x4 (&acc)[2][2][4][2], const Unit& u, int wr, int wc, int fr, int fq) const {
;     ...
;             for (int m = 0; m < 4; ++m) { const size_t r = (size_t)(row0 + ai * HALF + m * 16); float ss = 0.f;
; #pragma unroll
;                 for (int bj = 0; bj < 2; ++bj) { const size_t off = r * 4096 + col0 + bj * HALF;
;                     const f32x4 v0 = acc[ai][bj][m][0] * scale + *(const f32x4*)(R + off), v1 = acc[ai][bj][m][1] * scale + *(const f32x4*)(R + off + 4);
;                     ss += (v0[0] * v0[0] + v0[1] * v0[1]) + (v0[2] * v0[2] + v0[3] * v0[3]) + (v1[0] * v1[0] + v1[1] * v1[1]) + (v1[2] * v1[2] + v1[3] * v1[3]);
;                     u32x4 w; w.x = cvt_pk_bf16(v0[0], v0[1]); w.y = cvt_pk_bf16(v0[2], v0[3]); w.z = cvt_pk_bf16(v1[0], v1[1]); w.w = cvt_pk_bf16(v1[2], v1[3]);
;                     *(u32x4*)(HB + off) = w;
;                     u32x2e q; q.x = q8x4(v0, gv[bj][0], (float)HQS); q.y = q8x4(v1, gv[bj][1], (float)HQS);
;                     *(u32x2e*)(Q8 + r * LDQ8 + col0 + bj * HALF) = q; }
;                 ss += __shfl_xor(ss, 16); ss += __shfl_xor(ss, 32);
;                 if (fq == 0) SSQP[r * 64 + u.pn * 4 + wc] = ss; }
	v_lshlrev_b64 v[134:135], 8, v[140:141]
	v_lshl_add_u64 v[134:135], s[22:23], 0, v[134:135]
	s_waitcnt lgkmcnt(0)
	v_add_f32_e32 v130, v130, v131
	global_store_dword v[134:135], v130, off
.LBB0_619:
	s_or_b64 exec, exec, s[28:29]
	v_or_b32_e32 v130, 16, v140
	s_waitcnt lgkmcnt(0)
	v_ashrrev_i32_e32 v131, 31, v130
	v_lshlrev_b64 v[134:135], 12, v[130:131]
	v_lshl_add_u64 v[148:149], v[134:135], 0, v[138:139]
	v_lshl_add_u64 v[150:151], v[148:149], 2, s[8:9]
	global_load_dwordx4 v[134:137], v[150:151], off nt
	global_load_dwordx4 v[144:147], v[150:151], off offset:16 nt
	v_cvt_f32_i32_e32 v127, v127
	v_cvt_f32_i32_e32 v126, v126
	v_cvt_f32_i32_e32 v129, v129
	v_cvt_f32_i32_e32 v128, v128
	v_cvt_f32_i32_e32 v153, v123
	v_cvt_f32_i32_e32 v152, v122
	v_cvt_f32_i32_e32 v125, v125
	v_cvt_f32_i32_e32 v124, v124
	v_lshlrev_b64 v[148:149], 1, v[148:149]
	v_lshl_add_u64 v[154:155], s[14:15], 0, v[148:149]
	v_mad_i64_i32 v[122:123], s[28:29], v130, s50, v[142:143]
	v_cvt_f32_i32_e32 v119, v119
	v_cvt_f32_i32_e32 v118, v118
	v_cvt_f32_i32_e32 v121, v121
	v_cvt_f32_i32_e32 v120, v120
	v_cvt_f32_i32_e32 v115, v115
	v_cvt_f32_i32_e32 v114, v114
	v_cvt_f32_i32_e32 v117, v117
	v_cvt_f32_i32_e32 v116, v116
	v_or_b32_e32 v148, 0x100, v148
	v_lshl_add_u64 v[148:149], s[14:15], 0, v[148:149]
	s_waitcnt vmcnt(1)
	v_pk_fma_f32 v[128:129], v[128:129], s[26:27], v[136:137] op_sel_hi:[1,0,1]
	v_pk_fma_f32 v[156:157], v[126:127], s[26:27], v[134:135] op_sel_hi:[1,0,1]
	s_waitcnt vmcnt(0)
	v_pk_fma_f32 v[146:147], v[124:125], s[26:27], v[146:147] op_sel_hi:[1,0,1]
	v_pk_fma_f32 v[144:145], v[152:153], s[26:27], v[144:145] op_sel_hi:[1,0,1]
	v_cvt_pk_bf16_f32 v124, v156, v157
	v_cvt_pk_bf16_f32 v125, v128, v129
	v_mul_f32_e32 v134, v74, v156
	v_cvt_pk_bf16_f32 v126, v144, v145
	v_cvt_pk_bf16_f32 v127, v146, v147
	v_mul_f32_e32 v135, v75, v157
	v_mul_f32_e32 v136, v76, v128
	v_mul_f32_e32 v137, v77, v129
	v_mul_f32_e32 v141, v66, v144
	v_mul_f32_e32 v152, v67, v145
	v_mul_f32_e32 v153, v68, v146
	v_mul_f32_e32 v158, v69, v147
	global_store_dwordx4 v[154:155], v[124:127], off
	v_mul_f32_e32 v129, v129, v129
	v_fmac_f32_e32 v129, v128, v128
	v_mul_f32_e32 v124, 0x41c00000, v134
	v_mul_f32_e32 v125, 0x41c00000, v135
	v_mul_f32_e32 v126, 0x41c00000, v136
	v_mul_f32_e32 v127, 0x41c00000, v137
	v_mul_f32_e32 v134, 0x41c00000, v141
	v_mul_f32_e32 v135, 0x41c00000, v152
	v_mul_f32_e32 v136, 0x41c00000, v153
	v_mul_f32_e32 v137, 0x41c00000, v158
	v_med3_f32 v124, v124, s51, v177
	v_med3_f32 v125, v125, s51, v177
	v_med3_f32 v126, v126, s51, v177
	v_med3_f32 v127, v127, s51, v177
	v_med3_f32 v134, v134, s51, v177
	v_med3_f32 v135, v135, s51, v177
	v_med3_f32 v136, v136, s51, v177
	v_med3_f32 v137, v137, s51, v177
	v_add_f32_e32 v124, 0x4b400000, v124
	v_add_f32_e32 v125, 0x4b400000, v125
	v_add_f32_e32 v126, 0x4b400000, v126
	v_add_f32_e32 v127, 0x4b400000, v127
	v_add_f32_e32 v134, 0x4b400000, v134
	v_add_f32_e32 v135, 0x4b400000, v135
	v_add_f32_e32 v136, 0x4b400000, v136
	v_add_f32_e32 v137, 0x4b400000, v137
	v_perm_b32 v124, v125, v124, s56
	v_perm_b32 v125, v127, v126, s57
	v_perm_b32 v126, v135, v134, s56
	v_perm_b32 v127, v137, v136, s57
	v_or_b32_e32 v124, v124, v125
	v_or_b32_e32 v125, v126, v127
	global_store_dwordx2 v[122:123], v[124:125], off
	global_load_dwordx4 v[124:127], v[150:151], off offset:512 nt
	s_nop 0
	global_load_dwordx4 v[134:137], v[150:151], off offset:528 nt
	v_mul_f32_e32 v141, v157, v157
	v_fmac_f32_e32 v141, v156, v156
	v_add_f32_e32 v128, v141, v129
	v_mul_f32_e32 v145, v145, v145
	v_mul_f32_e32 v147, v147, v147
	v_fmac_f32_e32 v145, v144, v144
	v_fmac_f32_e32 v147, v146, v146
	v_add_f32_e32 v128, v128, v145
	v_add_f32_e32 v128, v147, v128
	s_waitcnt vmcnt(1)
	v_pk_fma_f32 v[120:121], v[120:121], s[26:27], v[126:127] op_sel_hi:[1,0,1]
	v_pk_fma_f32 v[118:119], v[118:119], s[26:27], v[124:125] op_sel_hi:[1,0,1]
	s_waitcnt vmcnt(0)
	v_pk_fma_f32 v[126:127], v[114:115], s[26:27], v[134:135] op_sel_hi:[1,0,1]
	v_mul_f32_e32 v129, v119, v119
	v_mul_f32_e32 v134, v121, v121
	v_pk_fma_f32 v[124:125], v[116:117], s[26:27], v[136:137] op_sel_hi:[1,0,1]
	v_mul_f32_e32 v135, v127, v127
	v_cvt_pk_bf16_f32 v114, v118, v119
	v_cvt_pk_bf16_f32 v115, v120, v121
	v_cvt_pk_bf16_f32 v116, v126, v127
	v_cvt_pk_bf16_f32 v117, v124, v125
	v_mul_f32_e32 v137, v62, v118
	v_mul_f32_e32 v119, v63, v119
	v_mul_f32_e32 v141, v64, v120
	v_mul_f32_e32 v121, v65, v121
	v_fmac_f32_e32 v129, v118, v118
	v_fmac_f32_e32 v134, v120, v120
	v_mul_f32_e32 v136, v125, v125
	v_fmac_f32_e32 v135, v126, v126
	global_store_dwordx4 v[148:149], v[114:117], off
	v_fmac_f32_e32 v136, v124, v124
	v_mul_f32_e32 v144, v50, v126
	v_mul_f32_e32 v114, 0x41c00000, v137
	v_mul_f32_e32 v115, 0x41c00000, v119
	v_mul_f32_e32 v116, 0x41c00000, v141
	v_mul_f32_e32 v117, 0x41c00000, v121
	v_add_f32_e32 v121, v129, v134
	v_med3_f32 v114, v114, s51, v177
	v_med3_f32 v115, v115, s51, v177
	v_med3_f32 v116, v116, s51, v177
	v_med3_f32 v117, v117, s51, v177
	v_add_f32_e32 v121, v121, v135
	v_add_f32_e32 v114, 0x4b400000, v114
	v_add_f32_e32 v115, 0x4b400000, v115
	v_add_f32_e32 v116, 0x4b400000, v116
	v_add_f32_e32 v117, 0x4b400000, v117
	v_add_f32_e32 v121, v136, v121
	v_perm_b32 v114, v115, v114, s56
	v_perm_b32 v115, v117, v116, s57
	v_add_f32_e32 v117, v128, v121
	v_or_b32_e32 v116, v114, v115
	ds_bpermute_b32 v114, v132, v117
	v_mul_f32_e32 v115, v53, v125
	v_mul_f32_e32 v115, 0x41c00000, v115
	v_mul_f32_e32 v127, v51, v127
	v_mul_f32_e32 v145, v52, v124
	v_med3_f32 v115, v115, s51, v177
	s_waitcnt lgkmcnt(0)
	v_add_f32_e32 v114, v117, v114
	v_mul_f32_e32 v118, 0x41c00000, v144
	v_mul_f32_e32 v119, 0x41c00000, v127
	v_mul_f32_e32 v120, 0x41c00000, v145
	v_add_f32_e32 v121, 0x4b400000, v115
	ds_bpermute_b32 v115, v133, v114
	v_med3_f32 v118, v118, s51, v177
	v_med3_f32 v119, v119, s51, v177
	v_med3_f32 v120, v120, s51, v177
	v_add_f32_e32 v118, 0x4b400000, v118
	v_add_f32_e32 v119, 0x4b400000, v119
	v_add_f32_e32 v120, 0x4b400000, v120
	v_perm_b32 v117, v119, v118, s56
	v_perm_b32 v118, v121, v120, s57
	v_or_b32_e32 v117, v117, v118
	global_store_dwordx2 v[122:123], v[116:117], off offset:128
	s_and_saveexec_b64 s[28:29], s[0:1]
	s_cbranch_execz .LBB0_621
	v_lshlrev_b64 v[116:117], 8, v[130:131]
	v_lshl_add_u64 v[116:117], s[22:23], 0, v[116:117]
	s_waitcnt lgkmcnt(0)
	v_add_f32_e32 v114, v114, v115
	global_store_dword v[116:117], v114, off
; __device__ __forceinline__ unsigned cvt_pk_bf16(float lo, float hi) { unsigned r; asm volatile("v_cvt_pk_bf16_f32 %0, %1, %2" : "=v"(r) : "v"(lo), "v"(hi)); return r; }
; __device__ __forceinline__ unsigned q8x4(const f32x4 a, const f32x4 g, float s) {
;     unsigned y[4];
; #pragma unroll
;     for (int i = 0; i < 4; ++i) y[i] = __float_as_uint(__builtin_fmaf(__builtin_amdgcn_fmed3f(a[i] * g[i] * s, -127.0f, 127.0f), 1.0f, 12582912.0f));
;     return __builtin_amdgcn_perm(y[1], y[0], 0x0c0c0400u) | __builtin_amdgcn_perm(y[3], y[2], 0x04000c0cu);
; }
;     __device__ __forceinline__ void operator()(const f32x4 (&acc)[2][2][4][2], const Unit& u, int wr, int wc, int fr, int fq) const {
;     ...
;             for (int m = 0; m < 4; ++m) { const size_t r = (size_t)(row0 + ai * HALF + m * 16); float ss = 0.f;
; #pragma unroll
;                 for (int bj = 0; bj < 2; ++bj) { const size_t off = r * 4096 + col0 + bj * HALF;
;                     const f32x4 v0 = acc[ai][bj][m][0] * scale + *(const f32x4*)(R + off), v1 = acc[ai][bj][m][1] * scale + *(const f32x4*)(R + off + 4);
;                     ss += (v0[0] * v0[0] + v0[1] * v0[1]) + (v0[2] * v0[2] + v0[3] * v0[3]) + (v1[0] * v1[0] + v1[1] * v1[1]) + (v1[2] * v1[2] + v1[3] * v1[3]);
;                     u32x4 w; w.x = cvt_pk_bf16(v0[0], v0[1]); w.y = cvt_pk_bf16(v0[2], v0[3]); w.z = cvt_pk_bf16(v1[0], v1[1]); w.w = cvt_pk_bf16(v1[2], v1[3]);
;                     *(u32x4*)(HB + off) = w;
;                     u32x2e q; q.x = q8x4(v0, gv[bj][0], (float)HQS); q.y = q8x4(v1, gv[bj][1], (float)HQS);
;                     *(u32x2e*)(Q8 + r * LDQ8 + col0 + bj * HALF) = q; }
;                 ss += __shfl_xor(ss, 16); ss += __shfl_xor(ss, 32);
;                 if (fq == 0) SSQP[r * 64 + u.pn * 4 + wc] = ss; }
.LBB0_621:
	s_or_b64 exec, exec, s[28:29]
	v_or_b32_e32 v114, 32, v140
	s_waitcnt lgkmcnt(0)
	v_ashrrev_i32_e32 v115, 31, v114
	v_lshlrev_b64 v[116:117], 12, v[114:115]
	v_lshl_add_u64 v[124:125], v[116:117], 0, v[138:139]
	v_lshl_add_u64 v[126:127], v[124:125], 2, s[8:9]
	global_load_dwordx4 v[116:119], v[126:127], off nt
	global_load_dwordx4 v[120:123], v[126:127], off offset:16 nt
	v_cvt_f32_i32_e32 v111, v111
	v_cvt_f32_i32_e32 v110, v110
	v_cvt_f32_i32_e32 v113, v113
	v_cvt_f32_i32_e32 v112, v112
	v_cvt_f32_i32_e32 v129, v107
	v_cvt_f32_i32_e32 v128, v106
	v_cvt_f32_i32_e32 v109, v109
	v_cvt_f32_i32_e32 v108, v108
	v_lshlrev_b64 v[124:125], 1, v[124:125]
	v_lshl_add_u64 v[130:131], s[14:15], 0, v[124:125]
	v_mad_i64_i32 v[106:107], s[28:29], v114, s50, v[142:143]
	v_cvt_f32_i32_e32 v103, v103
	v_cvt_f32_i32_e32 v102, v102
	v_cvt_f32_i32_e32 v105, v105
	v_cvt_f32_i32_e32 v104, v104
	v_cvt_f32_i32_e32 v99, v99
	v_cvt_f32_i32_e32 v98, v98
	v_cvt_f32_i32_e32 v101, v101
	v_cvt_f32_i32_e32 v100, v100
	v_or_b32_e32 v124, 0x100, v124
	v_lshl_add_u64 v[124:125], s[14:15], 0, v[124:125]
	s_waitcnt vmcnt(1)
	v_pk_fma_f32 v[112:113], v[112:113], s[26:27], v[118:119] op_sel_hi:[1,0,1]
	v_pk_fma_f32 v[134:135], v[110:111], s[26:27], v[116:117] op_sel_hi:[1,0,1]
	s_waitcnt vmcnt(0)
	v_pk_fma_f32 v[122:123], v[108:109], s[26:27], v[122:123] op_sel_hi:[1,0,1]
	v_pk_fma_f32 v[120:121], v[128:129], s[26:27], v[120:121] op_sel_hi:[1,0,1]
	v_cvt_pk_bf16_f32 v108, v134, v135
	v_cvt_pk_bf16_f32 v109, v112, v113
	v_mul_f32_e32 v116, v74, v134
	v_cvt_pk_bf16_f32 v110, v120, v121
	v_cvt_pk_bf16_f32 v111, v122, v123
	v_mul_f32_e32 v117, v75, v135
	v_mul_f32_e32 v118, v76, v112
	v_mul_f32_e32 v119, v77, v113
	v_mul_f32_e32 v128, v66, v120
	v_mul_f32_e32 v129, v67, v121
	v_mul_f32_e32 v136, v68, v122
	v_mul_f32_e32 v137, v69, v123
	global_store_dwordx4 v[130:131], v[108:111], off
	v_mul_f32_e32 v113, v113, v113
	v_fmac_f32_e32 v113, v112, v112
	v_mul_f32_e32 v108, 0x41c00000, v116
	v_mul_f32_e32 v109, 0x41c00000, v117
	v_mul_f32_e32 v110, 0x41c00000, v118
	v_mul_f32_e32 v111, 0x41c00000, v119
	v_mul_f32_e32 v116, 0x41c00000, v128
	v_mul_f32_e32 v117, 0x41c00000, v129
	v_mul_f32_e32 v118, 0x41c00000, v136
	v_mul_f32_e32 v119, 0x41c00000, v137
	v_med3_f32 v108, v108, s51, v177
	v_med3_f32 v109, v109, s51, v177
	v_med3_f32 v110, v110, s51, v177
	v_med3_f32 v111, v111, s51, v177
	v_med3_f32 v116, v116, s51, v177
	v_med3_f32 v117, v117, s51, v177
	v_med3_f32 v118, v118, s51, v177
	v_med3_f32 v119, v119, s51, v177
	v_add_f32_e32 v108, 0x4b400000, v108
	v_add_f32_e32 v109, 0x4b400000, v109
	v_add_f32_e32 v110, 0x4b400000, v110
	v_add_f32_e32 v111, 0x4b400000, v111
	v_add_f32_e32 v116, 0x4b400000, v116
	v_add_f32_e32 v117, 0x4b400000, v117
	v_add_f32_e32 v118, 0x4b400000, v118
	v_add_f32_e32 v119, 0x4b400000, v119
	v_perm_b32 v108, v109, v108, s56
	v_perm_b32 v109, v111, v110, s57
	v_perm_b32 v110, v117, v116, s56
	v_perm_b32 v111, v119, v118, s57
	v_or_b32_e32 v108, v108, v109
	v_or_b32_e32 v109, v110, v111
	global_store_dwordx2 v[106:107], v[108:109], off
	global_load_dwordx4 v[108:111], v[126:127], off offset:512 nt
	s_nop 0
	global_load_dwordx4 v[116:119], v[126:127], off offset:528 nt
	v_mul_f32_e32 v126, v135, v135
	v_fmac_f32_e32 v126, v134, v134
	v_mul_f32_e32 v121, v121, v121
	v_add_f32_e32 v112, v126, v113
	v_fmac_f32_e32 v121, v120, v120
	v_mul_f32_e32 v123, v123, v123
	v_fmac_f32_e32 v123, v122, v122
	v_add_f32_e32 v112, v112, v121
	v_add_f32_e32 v112, v123, v112
	s_waitcnt vmcnt(1)
	v_pk_fma_f32 v[104:105], v[104:105], s[26:27], v[110:111] op_sel_hi:[1,0,1]
	v_pk_fma_f32 v[102:103], v[102:103], s[26:27], v[108:109] op_sel_hi:[1,0,1]
	s_waitcnt vmcnt(0)
	v_pk_fma_f32 v[110:111], v[98:99], s[26:27], v[116:117] op_sel_hi:[1,0,1]
	v_mul_f32_e32 v113, v103, v103
	v_mul_f32_e32 v116, v105, v105
	v_pk_fma_f32 v[108:109], v[100:101], s[26:27], v[118:119] op_sel_hi:[1,0,1]
	v_mul_f32_e32 v117, v111, v111
	v_cvt_pk_bf16_f32 v98, v102, v103
	v_cvt_pk_bf16_f32 v99, v104, v105
	v_cvt_pk_bf16_f32 v100, v110, v111
	v_cvt_pk_bf16_f32 v101, v108, v109
	v_mul_f32_e32 v119, v62, v102
	v_mul_f32_e32 v103, v63, v103
	v_mul_f32_e32 v120, v64, v104
	v_mul_f32_e32 v105, v65, v105
	v_fmac_f32_e32 v113, v102, v102
	v_fmac_f32_e32 v116, v104, v104
	v_mul_f32_e32 v118, v109, v109
	v_fmac_f32_e32 v117, v110, v110
	global_store_dwordx4 v[124:125], v[98:101], off
	v_fmac_f32_e32 v118, v108, v108
	v_mul_f32_e32 v121, v50, v110
	v_mul_f32_e32 v98, 0x41c00000, v119
	v_mul_f32_e32 v99, 0x41c00000, v103
	v_mul_f32_e32 v100, 0x41c00000, v120
	v_mul_f32_e32 v101, 0x41c00000, v105
	v_add_f32_e32 v105, v113, v116
	v_med3_f32 v98, v98, s51, v177
	v_med3_f32 v99, v99, s51, v177
	v_med3_f32 v100, v100, s51, v177
	v_med3_f32 v101, v101, s51, v177
	v_add_f32_e32 v105, v105, v117
	v_add_f32_e32 v98, 0x4b400000, v98
	v_add_f32_e32 v99, 0x4b400000, v99
	v_add_f32_e32 v100, 0x4b400000, v100
	v_add_f32_e32 v101, 0x4b400000, v101
	v_add_f32_e32 v105, v118, v105
	v_perm_b32 v98, v99, v98, s56
	v_perm_b32 v99, v101, v100, s57
	v_add_f32_e32 v101, v112, v105
	v_or_b32_e32 v100, v98, v99
	ds_bpermute_b32 v98, v132, v101
	v_mul_f32_e32 v99, v53, v109
	v_mul_f32_e32 v99, 0x41c00000, v99
	v_mul_f32_e32 v111, v51, v111
	v_mul_f32_e32 v122, v52, v108
	v_med3_f32 v99, v99, s51, v177
	s_waitcnt lgkmcnt(0)
	v_add_f32_e32 v98, v101, v98
	v_mul_f32_e32 v102, 0x41c00000, v121
	v_mul_f32_e32 v103, 0x41c00000, v111
	v_mul_f32_e32 v104, 0x41c00000, v122
	v_add_f32_e32 v105, 0x4b400000, v99
	ds_bpermute_b32 v99, v133, v98
	v_med3_f32 v102, v102, s51, v177
	v_med3_f32 v103, v103, s51, v177
	v_med3_f32 v104, v104, s51, v177
	v_add_f32_e32 v102, 0x4b400000, v102
	v_add_f32_e32 v103, 0x4b400000, v103
	v_add_f32_e32 v104, 0x4b400000, v104
	v_perm_b32 v101, v103, v102, s56
	v_perm_b32 v102, v105, v104, s57
	v_or_b32_e32 v101, v101, v102
	global_store_dwordx2 v[106:107], v[100:101], off offset:128
	s_and_saveexec_b64 s[28:29], s[0:1]
	s_cbranch_execz .LBB0_623
	v_lshlrev_b64 v[100:101], 8, v[114:115]
	v_lshl_add_u64 v[100:101], s[22:23], 0, v[100:101]
	s_waitcnt lgkmcnt(0)
	v_add_f32_e32 v98, v98, v99
	global_store_dword v[100:101], v98, off
; __device__ __forceinline__ unsigned cvt_pk_bf16(float lo, float hi) { unsigned r; asm volatile("v_cvt_pk_bf16_f32 %0, %1, %2" : "=v"(r) : "v"(lo), "v"(hi)); return r; }
; __device__ __forceinline__ unsigned q8x4(const f32x4 a, const f32x4 g, float s) {
;     unsigned y[4];
; #pragma unroll
;     for (int i = 0; i < 4; ++i) y[i] = __float_as_uint(__builtin_fmaf(__builtin_amdgcn_fmed3f(a[i] * g[i] * s, -127.0f, 127.0f), 1.0f, 12582912.0f));
;     return __builtin_amdgcn_perm(y[1], y[0], 0x0c0c0400u) | __builtin_amdgcn_perm(y[3], y[2], 0x04000c0cu);
; }
;     __device__ __forceinline__ void operator()(const f32x4 (&acc)[2][2][4][2], const Unit& u, int wr, int wc, int fr, int fq) const {
;     ...
;             for (int m = 0; m < 4; ++m) { const size_t r = (size_t)(row0 + ai * HALF + m * 16); float ss = 0.f;
; #pragma unroll
;                 for (int bj = 0; bj < 2; ++bj) { const size_t off = r * 4096 + col0 + bj * HALF;
;                     const f32x4 v0 = acc[ai][bj][m][0] * scale + *(const f32x4*)(R + off), v1 = acc[ai][bj][m][1] * scale + *(const f32x4*)(R + off + 4);
;                     ss += (v0[0] * v0[0] + v0[1] * v0[1]) + (v0[2] * v0[2] + v0[3] * v0[3]) + (v1[0] * v1[0] + v1[1] * v1[1]) + (v1[2] * v1[2] + v1[3] * v1[3]);
;                     u32x4 w; w.x = cvt_pk_bf16(v0[0], v0[1]); w.y = cvt_pk_bf16(v0[2], v0[3]); w.z = cvt_pk_bf16(v1[0], v1[1]); w.w = cvt_pk_bf16(v1[2], v1[3]);
;                     *(u32x4*)(HB + off) = w;
;                     u32x2e q; q.x = q8x4(v0, gv[bj][0], (float)HQS); q.y = q8x4(v1, gv[bj][1], (float)HQS);
;                     *(u32x2e*)(Q8 + r * LDQ8 + col0 + bj * HALF) = q; }
;                 ss += __shfl_xor(ss, 16); ss += __shfl_xor(ss, 32);
;                 if (fq == 0) SSQP[r * 64 + u.pn * 4 + wc] = ss; }
.LBB0_623:
	s_or_b64 exec, exec, s[28:29]
	v_or_b32_e32 v98, 48, v140
	s_waitcnt lgkmcnt(0)
	v_ashrrev_i32_e32 v99, 31, v98
	v_lshlrev_b64 v[100:101], 12, v[98:99]
	v_lshl_add_u64 v[108:109], v[100:101], 0, v[138:139]
	v_lshl_add_u64 v[110:111], v[108:109], 2, s[8:9]
	global_load_dwordx4 v[100:103], v[110:111], off nt
	global_load_dwordx4 v[104:107], v[110:111], off offset:16 nt
	v_cvt_f32_i32_e32 v95, v95
	v_cvt_f32_i32_e32 v94, v94
	v_cvt_f32_i32_e32 v97, v97
	v_cvt_f32_i32_e32 v96, v96
	v_cvt_f32_i32_e32 v113, v91
	v_cvt_f32_i32_e32 v112, v90
	v_cvt_f32_i32_e32 v93, v93
	v_cvt_f32_i32_e32 v92, v92
	v_lshlrev_b64 v[108:109], 1, v[108:109]
	v_lshl_add_u64 v[114:115], s[14:15], 0, v[108:109]
	v_mad_i64_i32 v[90:91], s[28:29], v98, s50, v[142:143]
	v_cvt_f32_i32_e32 v87, v87
	v_cvt_f32_i32_e32 v86, v86
	v_cvt_f32_i32_e32 v89, v89
	v_cvt_f32_i32_e32 v88, v88
	v_cvt_f32_i32_e32 v83, v83
	v_cvt_f32_i32_e32 v82, v82
	v_cvt_f32_i32_e32 v85, v85
	v_cvt_f32_i32_e32 v84, v84
	v_or_b32_e32 v108, 0x100, v108
	v_lshl_add_u64 v[108:109], s[14:15], 0, v[108:109]
	s_waitcnt vmcnt(1)
	v_pk_fma_f32 v[96:97], v[96:97], s[26:27], v[102:103] op_sel_hi:[1,0,1]
	v_pk_fma_f32 v[116:117], v[94:95], s[26:27], v[100:101] op_sel_hi:[1,0,1]
	s_waitcnt vmcnt(0)
	v_pk_fma_f32 v[106:107], v[92:93], s[26:27], v[106:107] op_sel_hi:[1,0,1]
	v_pk_fma_f32 v[104:105], v[112:113], s[26:27], v[104:105] op_sel_hi:[1,0,1]
	v_cvt_pk_bf16_f32 v92, v116, v117
	v_cvt_pk_bf16_f32 v93, v96, v97
	v_mul_f32_e32 v100, v74, v116
	v_cvt_pk_bf16_f32 v94, v104, v105
	v_cvt_pk_bf16_f32 v95, v106, v107
	v_mul_f32_e32 v101, v75, v117
	v_mul_f32_e32 v102, v76, v96
	v_mul_f32_e32 v103, v77, v97
	v_mul_f32_e32 v112, v66, v104
	v_mul_f32_e32 v113, v67, v105
	v_mul_f32_e32 v118, v68, v106
	v_mul_f32_e32 v119, v69, v107
	global_store_dwordx4 v[114:115], v[92:95], off
	v_mul_f32_e32 v97, v97, v97
	v_fmac_f32_e32 v97, v96, v96
	v_mul_f32_e32 v92, 0x41c00000, v100
	v_mul_f32_e32 v93, 0x41c00000, v101
	v_mul_f32_e32 v94, 0x41c00000, v102
	v_mul_f32_e32 v95, 0x41c00000, v103
	v_mul_f32_e32 v100, 0x41c00000, v112
	v_mul_f32_e32 v101, 0x41c00000, v113
	v_mul_f32_e32 v102, 0x41c00000, v118
	v_mul_f32_e32 v103, 0x41c00000, v119
	v_med3_f32 v92, v92, s51, v177
	v_med3_f32 v93, v93, s51, v177
	v_med3_f32 v94, v94, s51, v177
	v_med3_f32 v95, v95, s51, v177
	v_med3_f32 v100, v100, s51, v177
	v_med3_f32 v101, v101, s51, v177
	v_med3_f32 v102, v102, s51, v177
	v_med3_f32 v103, v103, s51, v177
	v_add_f32_e32 v92, 0x4b400000, v92
	v_add_f32_e32 v93, 0x4b400000, v93
	v_add_f32_e32 v94, 0x4b400000, v94
	v_add_f32_e32 v95, 0x4b400000, v95
	v_add_f32_e32 v100, 0x4b400000, v100
	v_add_f32_e32 v101, 0x4b400000, v101
	v_add_f32_e32 v102, 0x4b400000, v102
	v_add_f32_e32 v103, 0x4b400000, v103
	v_perm_b32 v92, v93, v92, s56
	v_perm_b32 v93, v95, v94, s57
	v_perm_b32 v94, v101, v100, s56
	v_perm_b32 v95, v103, v102, s57
	v_or_b32_e32 v92, v92, v93
	v_or_b32_e32 v93, v94, v95
	global_store_dwordx2 v[90:91], v[92:93], off
	global_load_dwordx4 v[92:95], v[110:111], off offset:512 nt
	s_nop 0
	global_load_dwordx4 v[100:103], v[110:111], off offset:528 nt
	v_mul_f32_e32 v110, v117, v117
	v_fmac_f32_e32 v110, v116, v116
	v_mul_f32_e32 v105, v105, v105
	v_add_f32_e32 v96, v110, v97
	v_fmac_f32_e32 v105, v104, v104
	v_mul_f32_e32 v107, v107, v107
	v_fmac_f32_e32 v107, v106, v106
	v_add_f32_e32 v96, v96, v105
	v_add_f32_e32 v96, v107, v96
	s_waitcnt vmcnt(1)
	v_pk_fma_f32 v[88:89], v[88:89], s[26:27], v[94:95] op_sel_hi:[1,0,1]
	v_pk_fma_f32 v[86:87], v[86:87], s[26:27], v[92:93] op_sel_hi:[1,0,1]
	s_waitcnt vmcnt(0)
	v_pk_fma_f32 v[94:95], v[82:83], s[26:27], v[100:101] op_sel_hi:[1,0,1]
	v_mul_f32_e32 v97, v87, v87
	v_mul_f32_e32 v100, v89, v89
	v_pk_fma_f32 v[92:93], v[84:85], s[26:27], v[102:103] op_sel_hi:[1,0,1]
	v_mul_f32_e32 v101, v95, v95
	v_cvt_pk_bf16_f32 v82, v86, v87
	v_cvt_pk_bf16_f32 v83, v88, v89
	v_cvt_pk_bf16_f32 v84, v94, v95
	v_cvt_pk_bf16_f32 v85, v92, v93
	v_mul_f32_e32 v103, v62, v86
	v_mul_f32_e32 v87, v63, v87
	v_mul_f32_e32 v104, v64, v88
	v_mul_f32_e32 v89, v65, v89
	v_fmac_f32_e32 v97, v86, v86
	v_fmac_f32_e32 v100, v88, v88
	v_mul_f32_e32 v102, v93, v93
	v_fmac_f32_e32 v101, v94, v94
	global_store_dwordx4 v[108:109], v[82:85], off
	v_fmac_f32_e32 v102, v92, v92
	v_mul_f32_e32 v105, v50, v94
	v_mul_f32_e32 v82, 0x41c00000, v103
	v_mul_f32_e32 v83, 0x41c00000, v87
	v_mul_f32_e32 v84, 0x41c00000, v104
	v_mul_f32_e32 v85, 0x41c00000, v89
	v_add_f32_e32 v89, v97, v100
	v_med3_f32 v82, v82, s51, v177
	v_med3_f32 v83, v83, s51, v177
	v_med3_f32 v84, v84, s51, v177
	v_med3_f32 v85, v85, s51, v177
	v_add_f32_e32 v89, v89, v101
	v_add_f32_e32 v82, 0x4b400000, v82
	v_add_f32_e32 v83, 0x4b400000, v83
	v_add_f32_e32 v84, 0x4b400000, v84
	v_add_f32_e32 v85, 0x4b400000, v85
	v_add_f32_e32 v89, v102, v89
	v_perm_b32 v82, v83, v82, s56
	v_perm_b32 v83, v85, v84, s57
	v_add_f32_e32 v85, v96, v89
	v_or_b32_e32 v84, v82, v83
	ds_bpermute_b32 v82, v132, v85
	v_mul_f32_e32 v83, v53, v93
	v_mul_f32_e32 v83, 0x41c00000, v83
	v_mul_f32_e32 v95, v51, v95
	v_mul_f32_e32 v106, v52, v92
	v_med3_f32 v83, v83, s51, v177
	s_waitcnt lgkmcnt(0)
	v_add_f32_e32 v82, v85, v82
	v_mul_f32_e32 v86, 0x41c00000, v105
	v_mul_f32_e32 v87, 0x41c00000, v95
	v_mul_f32_e32 v88, 0x41c00000, v106
	v_add_f32_e32 v89, 0x4b400000, v83
	ds_bpermute_b32 v83, v133, v82
	v_med3_f32 v86, v86, s51, v177
	v_med3_f32 v87, v87, s51, v177
	v_med3_f32 v88, v88, s51, v177
	v_add_f32_e32 v86, 0x4b400000, v86
	v_add_f32_e32 v87, 0x4b400000, v87
	v_add_f32_e32 v88, 0x4b400000, v88
	v_perm_b32 v85, v87, v86, s56
	v_perm_b32 v86, v89, v88, s57
	v_or_b32_e32 v85, v85, v86
	global_store_dwordx2 v[90:91], v[84:85], off offset:128
	s_and_saveexec_b64 s[28:29], s[0:1]
	s_cbranch_execz .LBB0_625
	v_lshlrev_b64 v[84:85], 8, v[98:99]
	v_lshl_add_u64 v[84:85], s[22:23], 0, v[84:85]
	s_waitcnt lgkmcnt(0)
	v_add_f32_e32 v82, v82, v83
	global_store_dword v[84:85], v82, off
; __device__ __forceinline__ unsigned cvt_pk_bf16(float lo, float hi) { unsigned r; asm volatile("v_cvt_pk_bf16_f32 %0, %1, %2" : "=v"(r) : "v"(lo), "v"(hi)); return r; }
; __device__ __forceinline__ unsigned q8x4(const f32x4 a, const f32x4 g, float s) {
;     unsigned y[4];
; #pragma unroll
;     for (int i = 0; i < 4; ++i) y[i] = __float_as_uint(__builtin_fmaf(__builtin_amdgcn_fmed3f(a[i] * g[i] * s, -127.0f, 127.0f), 1.0f, 12582912.0f));
;     return __builtin_amdgcn_perm(y[1], y[0], 0x0c0c0400u) | __builtin_amdgcn_perm(y[3], y[2], 0x04000c0cu);
; }
;     __device__ __forceinline__ void operator()(const f32x4 (&acc)[2][2][4][2], const Unit& u, int wr, int wc, int fr, int fq) const {
;     ...
;             for (int m = 0; m < 4; ++m) { const size_t r = (size_t)(row0 + ai * HALF + m * 16); float ss = 0.f;
; #pragma unroll
;                 for (int bj = 0; bj < 2; ++bj) { const size_t off = r * 4096 + col0 + bj * HALF;
;                     const f32x4 v0 = acc[ai][bj][m][0] * scale + *(const f32x4*)(R + off), v1 = acc[ai][bj][m][1] * scale + *(const f32x4*)(R + off + 4);
;                     ss += (v0[0] * v0[0] + v0[1] * v0[1]) + (v0[2] * v0[2] + v0[3] * v0[3]) + (v1[0] * v1[0] + v1[1] * v1[1]) + (v1[2] * v1[2] + v1[3] * v1[3]);
;                     u32x4 w; w.x = cvt_pk_bf16(v0[0], v0[1]); w.y = cvt_pk_bf16(v0[2], v0[3]); w.z = cvt_pk_bf16(v1[0], v1[1]); w.w = cvt_pk_bf16(v1[2], v1[3]);
;                     *(u32x4*)(HB + off) = w;
;                     u32x2e q; q.x = q8x4(v0, gv[bj][0], (float)HQS); q.y = q8x4(v1, gv[bj][1], (float)HQS);
;                     *(u32x2e*)(Q8 + r * LDQ8 + col0 + bj * HALF) = q; }
;                 ss += __shfl_xor(ss, 16); ss += __shfl_xor(ss, 32);
;                 if (fq == 0) SSQP[r * 64 + u.pn * 4 + wc] = ss; }
.LBB0_625:
	s_or_b64 exec, exec, s[28:29]
	v_add_u32_e32 v82, 0x80, v140
	s_waitcnt lgkmcnt(0)
	v_ashrrev_i32_e32 v83, 31, v82
	v_lshlrev_b64 v[84:85], 12, v[82:83]
	v_lshl_add_u64 v[92:93], v[84:85], 0, v[138:139]
	v_lshl_add_u64 v[94:95], v[92:93], 2, s[8:9]
	global_load_dwordx4 v[84:87], v[94:95], off nt
	global_load_dwordx4 v[88:91], v[94:95], off offset:16 nt
	v_cvt_f32_i32_e32 v79, v79
	v_cvt_f32_i32_e32 v78, v78
	v_cvt_f32_i32_e32 v81, v81
	v_cvt_f32_i32_e32 v80, v80
	v_cvt_f32_i32_e32 v97, v71
	v_cvt_f32_i32_e32 v96, v70
	v_cvt_f32_i32_e32 v73, v73
	v_cvt_f32_i32_e32 v72, v72
	v_lshlrev_b64 v[92:93], 1, v[92:93]
	v_lshl_add_u64 v[98:99], s[14:15], 0, v[92:93]
	v_mad_i64_i32 v[70:71], s[28:29], v82, s50, v[142:143]
	v_cvt_f32_i32_e32 v59, v59
	v_cvt_f32_i32_e32 v58, v58
	v_cvt_f32_i32_e32 v61, v61
	v_cvt_f32_i32_e32 v60, v60
	v_cvt_f32_i32_e32 v55, v55
	v_cvt_f32_i32_e32 v54, v54
	v_or_b32_e32 v92, 0x100, v92
	v_cvt_f32_i32_e32 v57, v57
	v_cvt_f32_i32_e32 v56, v56
	s_waitcnt vmcnt(1)
	v_pk_fma_f32 v[100:101], v[80:81], s[26:27], v[86:87] op_sel_hi:[1,0,1]
	v_pk_fma_f32 v[102:103], v[78:79], s[26:27], v[84:85] op_sel_hi:[1,0,1]
	s_waitcnt vmcnt(0)
	v_pk_fma_f32 v[72:73], v[72:73], s[26:27], v[90:91] op_sel_hi:[1,0,1]
	v_pk_fma_f32 v[88:89], v[96:97], s[26:27], v[88:89] op_sel_hi:[1,0,1]
	v_cvt_pk_bf16_f32 v78, v102, v103
	v_cvt_pk_bf16_f32 v79, v100, v101
	v_mul_f32_e32 v84, v74, v102
	v_cvt_pk_bf16_f32 v80, v88, v89
	v_cvt_pk_bf16_f32 v81, v72, v73
	v_mul_f32_e32 v85, v75, v103
	v_mul_f32_e32 v86, v76, v100
	v_mul_f32_e32 v87, v77, v101
	v_mul_f32_e32 v90, v66, v88
	v_mul_f32_e32 v91, v67, v89
	v_mul_f32_e32 v96, v68, v72
	v_mul_f32_e32 v97, v69, v73
	global_store_dwordx4 v[98:99], v[78:81], off
	v_mul_f32_e32 v89, v89, v89
	v_mul_f32_e32 v73, v73, v73
	v_mul_f32_e32 v78, 0x41c00000, v84
	v_mul_f32_e32 v79, 0x41c00000, v85
	v_mul_f32_e32 v80, 0x41c00000, v86
	v_mul_f32_e32 v81, 0x41c00000, v87
	v_mul_f32_e32 v84, 0x41c00000, v90
	v_mul_f32_e32 v85, 0x41c00000, v91
	v_mul_f32_e32 v86, 0x41c00000, v96
	v_mul_f32_e32 v87, 0x41c00000, v97
	v_med3_f32 v78, v78, s51, v177
	v_med3_f32 v79, v79, s51, v177
	v_med3_f32 v80, v80, s51, v177
	v_med3_f32 v81, v81, s51, v177
	v_med3_f32 v84, v84, s51, v177
	v_med3_f32 v85, v85, s51, v177
	v_med3_f32 v86, v86, s51, v177
	v_med3_f32 v87, v87, s51, v177
	v_add_f32_e32 v78, 0x4b400000, v78
	v_add_f32_e32 v79, 0x4b400000, v79
	v_add_f32_e32 v80, 0x4b400000, v80
	v_add_f32_e32 v81, 0x4b400000, v81
	v_add_f32_e32 v84, 0x4b400000, v84
	v_add_f32_e32 v85, 0x4b400000, v85
	v_add_f32_e32 v86, 0x4b400000, v86
	v_add_f32_e32 v87, 0x4b400000, v87
	v_perm_b32 v78, v79, v78, s56
	v_perm_b32 v79, v81, v80, s57
	v_perm_b32 v80, v85, v84, s56
	v_perm_b32 v81, v87, v86, s57
	v_or_b32_e32 v78, v78, v79
	v_or_b32_e32 v79, v80, v81
	global_store_dwordx2 v[70:71], v[78:79], off
	global_load_dwordx4 v[78:81], v[94:95], off offset:512 nt
	s_nop 0
	global_load_dwordx4 v[84:87], v[94:95], off offset:528 nt
	v_lshl_add_u64 v[90:91], s[14:15], 0, v[92:93]
	v_mul_f32_e32 v92, v103, v103
	v_mul_f32_e32 v93, v101, v101
	v_fmac_f32_e32 v92, v102, v102
	v_fmac_f32_e32 v93, v100, v100
	v_fmac_f32_e32 v89, v88, v88
	v_fmac_f32_e32 v73, v72, v72
	v_add_f32_e32 v72, v92, v93
	v_add_f32_e32 v72, v72, v89
	v_add_f32_e32 v88, v73, v72
	s_waitcnt vmcnt(1)
	v_pk_fma_f32 v[60:61], v[60:61], s[26:27], v[80:81] op_sel_hi:[1,0,1]
	v_pk_fma_f32 v[58:59], v[58:59], s[26:27], v[78:79] op_sel_hi:[1,0,1]
	s_waitcnt vmcnt(0)
	v_pk_fma_f32 v[78:79], v[54:55], s[26:27], v[84:85] op_sel_hi:[1,0,1]
	v_mul_f32_e32 v80, v59, v59
	v_mul_f32_e32 v81, v61, v61
	v_pk_fma_f32 v[72:73], v[56:57], s[26:27], v[86:87] op_sel_hi:[1,0,1]
	v_mul_f32_e32 v84, v79, v79
	v_cvt_pk_bf16_f32 v54, v58, v59
	v_cvt_pk_bf16_f32 v55, v60, v61
	v_cvt_pk_bf16_f32 v56, v78, v79
	v_cvt_pk_bf16_f32 v57, v72, v73
	v_mul_f32_e32 v86, v62, v58
	v_mul_f32_e32 v59, v63, v59
	v_mul_f32_e32 v87, v64, v60
	v_mul_f32_e32 v61, v65, v61
	v_fmac_f32_e32 v80, v58, v58
	v_fmac_f32_e32 v81, v60, v60
	v_mul_f32_e32 v85, v73, v73
	v_fmac_f32_e32 v84, v78, v78
	global_store_dwordx4 v[90:91], v[54:57], off
	v_fmac_f32_e32 v85, v72, v72
	v_mul_f32_e32 v89, v50, v78
	v_mul_f32_e32 v54, 0x41c00000, v86
	v_mul_f32_e32 v55, 0x41c00000, v59
	v_mul_f32_e32 v56, 0x41c00000, v87
	v_mul_f32_e32 v57, 0x41c00000, v61
	v_add_f32_e32 v61, v80, v81
	v_med3_f32 v54, v54, s51, v177
	v_med3_f32 v55, v55, s51, v177
	v_med3_f32 v56, v56, s51, v177
	v_med3_f32 v57, v57, s51, v177
	v_add_f32_e32 v61, v61, v84
	v_add_f32_e32 v54, 0x4b400000, v54
	v_add_f32_e32 v55, 0x4b400000, v55
	v_add_f32_e32 v56, 0x4b400000, v56
	v_add_f32_e32 v57, 0x4b400000, v57
	v_add_f32_e32 v61, v85, v61
	v_perm_b32 v54, v55, v54, s56
	v_perm_b32 v55, v57, v56, s57
	v_add_f32_e32 v57, v88, v61
	v_or_b32_e32 v56, v54, v55
	ds_bpermute_b32 v54, v132, v57
	v_mul_f32_e32 v55, v53, v73
	v_mul_f32_e32 v55, 0x41c00000, v55
	v_mul_f32_e32 v79, v51, v79
	v_mul_f32_e32 v92, v52, v72
	v_med3_f32 v55, v55, s51, v177
	s_waitcnt lgkmcnt(0)
	v_add_f32_e32 v54, v57, v54
	v_mul_f32_e32 v58, 0x41c00000, v89
	v_mul_f32_e32 v59, 0x41c00000, v79
	v_mul_f32_e32 v60, 0x41c00000, v92
	v_add_f32_e32 v61, 0x4b400000, v55
	ds_bpermute_b32 v55, v133, v54
	v_med3_f32 v58, v58, s51, v177
	v_med3_f32 v59, v59, s51, v177
	v_med3_f32 v60, v60, s51, v177
	v_add_f32_e32 v58, 0x4b400000, v58
	v_add_f32_e32 v59, 0x4b400000, v59
	v_add_f32_e32 v60, 0x4b400000, v60
	v_perm_b32 v57, v59, v58, s56
	v_perm_b32 v58, v61, v60, s57
	v_or_b32_e32 v57, v57, v58
	global_store_dwordx2 v[70:71], v[56:57], off offset:128
	s_and_saveexec_b64 s[28:29], s[0:1]
	s_cbranch_execz .LBB0_627
	v_lshlrev_b64 v[56:57], 8, v[82:83]
	v_lshl_add_u64 v[56:57], s[22:23], 0, v[56:57]
	s_waitcnt lgkmcnt(0)
	v_add_f32_e32 v54, v54, v55
	global_store_dword v[56:57], v54, off
; __device__ __forceinline__ unsigned cvt_pk_bf16(float lo, float hi) { unsigned r; asm volatile("v_cvt_pk_bf16_f32 %0, %1, %2" : "=v"(r) : "v"(lo), "v"(hi)); return r; }
; __device__ __forceinline__ unsigned q8x4(const f32x4 a, const f32x4 g, float s) {
;     unsigned y[4];
; #pragma unroll
;     for (int i = 0; i < 4; ++i) y[i] = __float_as_uint(__builtin_fmaf(__builtin_amdgcn_fmed3f(a[i] * g[i] * s, -127.0f, 127.0f), 1.0f, 12582912.0f));
;     return __builtin_amdgcn_perm(y[1], y[0], 0x0c0c0400u) | __builtin_amdgcn_perm(y[3], y[2], 0x04000c0cu);
; }
;     __device__ __forceinline__ void operator()(const f32x4 (&acc)[2][2][4][2], const Unit& u, int wr, int wc, int fr, int fq) const {
;     ...
;             for (int m = 0; m < 4; ++m) { const size_t r = (size_t)(row0 + ai * HALF + m * 16); float ss = 0.f;
; #pragma unroll
;                 for (int bj = 0; bj < 2; ++bj) { const size_t off = r * 4096 + col0 + bj * HALF;
;                     const f32x4 v0 = acc[ai][bj][m][0] * scale + *(const f32x4*)(R + off), v1 = acc[ai][bj][m][1] * scale + *(const f32x4*)(R + off + 4);
;                     ss += (v0[0] * v0[0] + v0[1] * v0[1]) + (v0[2] * v0[2] + v0[3] * v0[3]) + (v1[0] * v1[0] + v1[1] * v1[1]) + (v1[2] * v1[2] + v1[3] * v1[3]);
;                     u32x4 w; w.x = cvt_pk_bf16(v0[0], v0[1]); w.y = cvt_pk_bf16(v0[2], v0[3]); w.z = cvt_pk_bf16(v1[0], v1[1]); w.w = cvt_pk_bf16(v1[2], v1[3]);
;                     *(u32x4*)(HB + off) = w;
;                     u32x2e q; q.x = q8x4(v0, gv[bj][0], (float)HQS); q.y = q8x4(v1, gv[bj][1], (float)HQS);
;                     *(u32x2e*)(Q8 + r * LDQ8 + col0 + bj * HALF) = q; }
;                 ss += __shfl_xor(ss, 16); ss += __shfl_xor(ss, 32);
;                 if (fq == 0) SSQP[r * 64 + u.pn * 4 + wc] = ss; }
.LBB0_627:
	s_or_b64 exec, exec, s[28:29]
	v_add_u32_e32 v54, 0x90, v140
	s_waitcnt lgkmcnt(0)
	v_ashrrev_i32_e32 v55, 31, v54
	v_lshlrev_b64 v[56:57], 12, v[54:55]
	v_lshl_add_u64 v[60:61], v[56:57], 0, v[138:139]
	v_lshl_add_u64 v[78:79], v[60:61], 2, s[8:9]
	global_load_dwordx4 v[56:59], v[78:79], off nt
	global_load_dwordx4 v[70:73], v[78:79], off offset:16 nt
	v_cvt_f32_i32_e32 v47, v47
	v_cvt_f32_i32_e32 v46, v46
	v_cvt_f32_i32_e32 v49, v49
	v_cvt_f32_i32_e32 v48, v48
	v_cvt_f32_i32_e32 v81, v43
	v_cvt_f32_i32_e32 v80, v42
	v_cvt_f32_i32_e32 v45, v45
	v_cvt_f32_i32_e32 v44, v44
	v_lshlrev_b64 v[60:61], 1, v[60:61]
	v_lshl_add_u64 v[82:83], s[14:15], 0, v[60:61]
	v_mad_i64_i32 v[42:43], s[28:29], v54, s50, v[142:143]
	v_cvt_f32_i32_e32 v39, v39
	v_cvt_f32_i32_e32 v38, v38
	v_cvt_f32_i32_e32 v41, v41
	v_cvt_f32_i32_e32 v40, v40
	v_cvt_f32_i32_e32 v35, v35
	v_cvt_f32_i32_e32 v34, v34
	v_cvt_f32_i32_e32 v37, v37
	v_cvt_f32_i32_e32 v36, v36
	v_or_b32_e32 v60, 0x100, v60
	v_lshl_add_u64 v[60:61], s[14:15], 0, v[60:61]
	s_waitcnt vmcnt(1)
	v_pk_fma_f32 v[48:49], v[48:49], s[26:27], v[58:59] op_sel_hi:[1,0,1]
	v_pk_fma_f32 v[84:85], v[46:47], s[26:27], v[56:57] op_sel_hi:[1,0,1]
	s_waitcnt vmcnt(0)
	v_pk_fma_f32 v[72:73], v[44:45], s[26:27], v[72:73] op_sel_hi:[1,0,1]
	v_pk_fma_f32 v[70:71], v[80:81], s[26:27], v[70:71] op_sel_hi:[1,0,1]
	v_cvt_pk_bf16_f32 v44, v84, v85
	v_cvt_pk_bf16_f32 v45, v48, v49
	v_mul_f32_e32 v56, v74, v84
	v_cvt_pk_bf16_f32 v46, v70, v71
	v_cvt_pk_bf16_f32 v47, v72, v73
	v_mul_f32_e32 v57, v75, v85
	v_mul_f32_e32 v58, v76, v48
	v_mul_f32_e32 v59, v77, v49
	v_mul_f32_e32 v80, v66, v70
	v_mul_f32_e32 v81, v67, v71
	v_mul_f32_e32 v86, v68, v72
	v_mul_f32_e32 v87, v69, v73
	global_store_dwordx4 v[82:83], v[44:47], off
	v_mul_f32_e32 v49, v49, v49
	v_fmac_f32_e32 v49, v48, v48
	v_mul_f32_e32 v44, 0x41c00000, v56
	v_mul_f32_e32 v45, 0x41c00000, v57
	v_mul_f32_e32 v46, 0x41c00000, v58
	v_mul_f32_e32 v47, 0x41c00000, v59
	v_mul_f32_e32 v56, 0x41c00000, v80
	v_mul_f32_e32 v57, 0x41c00000, v81
	v_mul_f32_e32 v58, 0x41c00000, v86
	v_mul_f32_e32 v59, 0x41c00000, v87
	v_med3_f32 v44, v44, s51, v177
	v_med3_f32 v45, v45, s51, v177
	v_med3_f32 v46, v46, s51, v177
	v_med3_f32 v47, v47, s51, v177
	v_med3_f32 v56, v56, s51, v177
	v_med3_f32 v57, v57, s51, v177
	v_med3_f32 v58, v58, s51, v177
	v_med3_f32 v59, v59, s51, v177
	v_add_f32_e32 v44, 0x4b400000, v44
	v_add_f32_e32 v45, 0x4b400000, v45
	v_add_f32_e32 v46, 0x4b400000, v46
	v_add_f32_e32 v47, 0x4b400000, v47
	v_add_f32_e32 v56, 0x4b400000, v56
	v_add_f32_e32 v57, 0x4b400000, v57
	v_add_f32_e32 v58, 0x4b400000, v58
	v_add_f32_e32 v59, 0x4b400000, v59
	v_perm_b32 v44, v45, v44, s56
	v_perm_b32 v45, v47, v46, s57
	v_perm_b32 v46, v57, v56, s56
	v_perm_b32 v47, v59, v58, s57
	v_or_b32_e32 v44, v44, v45
	v_or_b32_e32 v45, v46, v47
	global_store_dwordx2 v[42:43], v[44:45], off
	global_load_dwordx4 v[44:47], v[78:79], off offset:512 nt
	s_nop 0
	global_load_dwordx4 v[56:59], v[78:79], off offset:528 nt
	v_mul_f32_e32 v78, v85, v85
	v_fmac_f32_e32 v78, v84, v84
	v_mul_f32_e32 v71, v71, v71
	v_add_f32_e32 v48, v78, v49
	v_fmac_f32_e32 v71, v70, v70
	v_mul_f32_e32 v73, v73, v73
	v_fmac_f32_e32 v73, v72, v72
	v_add_f32_e32 v48, v48, v71
	v_add_f32_e32 v48, v73, v48
	s_waitcnt vmcnt(1)
	v_pk_fma_f32 v[40:41], v[40:41], s[26:27], v[46:47] op_sel_hi:[1,0,1]
	v_pk_fma_f32 v[38:39], v[38:39], s[26:27], v[44:45] op_sel_hi:[1,0,1]
	s_waitcnt vmcnt(0)
	v_pk_fma_f32 v[46:47], v[34:35], s[26:27], v[56:57] op_sel_hi:[1,0,1]
	v_mul_f32_e32 v49, v39, v39
	v_mul_f32_e32 v56, v41, v41
	v_pk_fma_f32 v[44:45], v[36:37], s[26:27], v[58:59] op_sel_hi:[1,0,1]
	v_mul_f32_e32 v57, v47, v47
	v_cvt_pk_bf16_f32 v34, v38, v39
	v_cvt_pk_bf16_f32 v35, v40, v41
	v_cvt_pk_bf16_f32 v36, v46, v47
	v_cvt_pk_bf16_f32 v37, v44, v45
	v_mul_f32_e32 v59, v62, v38
	v_mul_f32_e32 v39, v63, v39
	v_mul_f32_e32 v70, v64, v40
	v_mul_f32_e32 v41, v65, v41
	v_fmac_f32_e32 v49, v38, v38
	v_fmac_f32_e32 v56, v40, v40
	v_mul_f32_e32 v58, v45, v45
	v_fmac_f32_e32 v57, v46, v46
	global_store_dwordx4 v[60:61], v[34:37], off
	v_fmac_f32_e32 v58, v44, v44
	v_mul_f32_e32 v71, v50, v46
	v_mul_f32_e32 v34, 0x41c00000, v59
	v_mul_f32_e32 v35, 0x41c00000, v39
	v_mul_f32_e32 v36, 0x41c00000, v70
	v_mul_f32_e32 v37, 0x41c00000, v41
	v_add_f32_e32 v41, v49, v56
	v_med3_f32 v34, v34, s51, v177
	v_med3_f32 v35, v35, s51, v177
	v_med3_f32 v36, v36, s51, v177
	v_med3_f32 v37, v37, s51, v177
	v_add_f32_e32 v41, v41, v57
	v_add_f32_e32 v34, 0x4b400000, v34
	v_add_f32_e32 v35, 0x4b400000, v35
	v_add_f32_e32 v36, 0x4b400000, v36
	v_add_f32_e32 v37, 0x4b400000, v37
	v_add_f32_e32 v41, v58, v41
	v_perm_b32 v34, v35, v34, s56
	v_perm_b32 v35, v37, v36, s57
	v_add_f32_e32 v37, v48, v41
	v_or_b32_e32 v36, v34, v35
	ds_bpermute_b32 v34, v132, v37
	v_mul_f32_e32 v35, v53, v45
	v_mul_f32_e32 v35, 0x41c00000, v35
	v_mul_f32_e32 v47, v51, v47
	v_mul_f32_e32 v72, v52, v44
	v_med3_f32 v35, v35, s51, v177
	s_waitcnt lgkmcnt(0)
	v_add_f32_e32 v34, v37, v34
	v_mul_f32_e32 v38, 0x41c00000, v71
	v_mul_f32_e32 v39, 0x41c00000, v47
	v_mul_f32_e32 v40, 0x41c00000, v72
	v_add_f32_e32 v41, 0x4b400000, v35
	ds_bpermute_b32 v35, v133, v34
	v_med3_f32 v38, v38, s51, v177
	v_med3_f32 v39, v39, s51, v177
	v_med3_f32 v40, v40, s51, v177
	v_add_f32_e32 v38, 0x4b400000, v38
	v_add_f32_e32 v39, 0x4b400000, v39
	v_add_f32_e32 v40, 0x4b400000, v40
	v_perm_b32 v37, v39, v38, s56
	v_perm_b32 v38, v41, v40, s57
	v_or_b32_e32 v37, v37, v38
	global_store_dwordx2 v[42:43], v[36:37], off offset:128
	s_and_saveexec_b64 s[28:29], s[0:1]
	s_cbranch_execz .LBB0_629
	v_lshlrev_b64 v[36:37], 8, v[54:55]
	v_lshl_add_u64 v[36:37], s[22:23], 0, v[36:37]
	s_waitcnt lgkmcnt(0)
	v_add_f32_e32 v34, v34, v35
	global_store_dword v[36:37], v34, off
; __device__ __forceinline__ unsigned cvt_pk_bf16(float lo, float hi) { unsigned r; asm volatile("v_cvt_pk_bf16_f32 %0, %1, %2" : "=v"(r) : "v"(lo), "v"(hi)); return r; }
; __device__ __forceinline__ unsigned q8x4(const f32x4 a, const f32x4 g, float s) {
;     unsigned y[4];
; #pragma unroll
;     for (int i = 0; i < 4; ++i) y[i] = __float_as_uint(__builtin_fmaf(__builtin_amdgcn_fmed3f(a[i] * g[i] * s, -127.0f, 127.0f), 1.0f, 12582912.0f));
;     return __builtin_amdgcn_perm(y[1], y[0], 0x0c0c0400u) | __builtin_amdgcn_perm(y[3], y[2], 0x04000c0cu);
; }
;     __device__ __forceinline__ void operator()(const f32x4 (&acc)[2][2][4][2], const Unit& u, int wr, int wc, int fr, int fq) const {
;     ...
;             for (int m = 0; m < 4; ++m) { const size_t r = (size_t)(row0 + ai * HALF + m * 16); float ss = 0.f;
; #pragma unroll
;                 for (int bj = 0; bj < 2; ++bj) { const size_t off = r * 4096 + col0 + bj * HALF;
;                     const f32x4 v0 = acc[ai][bj][m][0] * scale + *(const f32x4*)(R + off), v1 = acc[ai][bj][m][1] * scale + *(const f32x4*)(R + off + 4);
;                     ss += (v0[0] * v0[0] + v0[1] * v0[1]) + (v0[2] * v0[2] + v0[3] * v0[3]) + (v1[0] * v1[0] + v1[1] * v1[1]) + (v1[2] * v1[2] + v1[3] * v1[3]);
;                     u32x4 w; w.x = cvt_pk_bf16(v0[0], v0[1]); w.y = cvt_pk_bf16(v0[2], v0[3]); w.z = cvt_pk_bf16(v1[0], v1[1]); w.w = cvt_pk_bf16(v1[2], v1[3]);
;                     *(u32x4*)(HB + off) = w;
;                     u32x2e q; q.x = q8x4(v0, gv[bj][0], (float)HQS); q.y = q8x4(v1, gv[bj][1], (float)HQS);
;                     *(u32x2e*)(Q8 + r * LDQ8 + col0 + bj * HALF) = q; }
;                 ss += __shfl_xor(ss, 16); ss += __shfl_xor(ss, 32);
;                 if (fq == 0) SSQP[r * 64 + u.pn * 4 + wc] = ss; }
.LBB0_629:
	s_or_b64 exec, exec, s[28:29]
	v_add_u32_e32 v34, 0xa0, v140
	s_waitcnt lgkmcnt(0)
	v_ashrrev_i32_e32 v35, 31, v34
	v_lshlrev_b64 v[36:37], 12, v[34:35]
	v_lshl_add_u64 v[44:45], v[36:37], 0, v[138:139]
	v_lshl_add_u64 v[46:47], v[44:45], 2, s[8:9]
	global_load_dwordx4 v[36:39], v[46:47], off nt
	global_load_dwordx4 v[40:43], v[46:47], off offset:16 nt
	v_cvt_f32_i32_e32 v31, v31
	v_cvt_f32_i32_e32 v30, v30
	v_cvt_f32_i32_e32 v33, v33
	v_cvt_f32_i32_e32 v32, v32
	v_cvt_f32_i32_e32 v49, v27
	v_cvt_f32_i32_e32 v48, v26
	v_cvt_f32_i32_e32 v29, v29
	v_cvt_f32_i32_e32 v28, v28
	v_lshlrev_b64 v[44:45], 1, v[44:45]
	v_lshl_add_u64 v[54:55], s[14:15], 0, v[44:45]
	v_mad_i64_i32 v[26:27], s[28:29], v34, s50, v[142:143]
	v_cvt_f32_i32_e32 v23, v23
	v_cvt_f32_i32_e32 v22, v22
	v_cvt_f32_i32_e32 v25, v25
	v_cvt_f32_i32_e32 v24, v24
	v_cvt_f32_i32_e32 v19, v19
	v_cvt_f32_i32_e32 v18, v18
	v_cvt_f32_i32_e32 v21, v21
	v_cvt_f32_i32_e32 v20, v20
	v_or_b32_e32 v44, 0x100, v44
	v_lshl_add_u64 v[44:45], s[14:15], 0, v[44:45]
	s_waitcnt vmcnt(1)
	v_pk_fma_f32 v[32:33], v[32:33], s[26:27], v[38:39] op_sel_hi:[1,0,1]
	v_pk_fma_f32 v[56:57], v[30:31], s[26:27], v[36:37] op_sel_hi:[1,0,1]
	s_waitcnt vmcnt(0)
	v_pk_fma_f32 v[42:43], v[28:29], s[26:27], v[42:43] op_sel_hi:[1,0,1]
	v_pk_fma_f32 v[40:41], v[48:49], s[26:27], v[40:41] op_sel_hi:[1,0,1]
	v_cvt_pk_bf16_f32 v28, v56, v57
	v_cvt_pk_bf16_f32 v29, v32, v33
	v_mul_f32_e32 v36, v74, v56
	v_cvt_pk_bf16_f32 v30, v40, v41
	v_cvt_pk_bf16_f32 v31, v42, v43
	v_mul_f32_e32 v37, v75, v57
	v_mul_f32_e32 v38, v76, v32
	v_mul_f32_e32 v39, v77, v33
	v_mul_f32_e32 v48, v66, v40
	v_mul_f32_e32 v49, v67, v41
	v_mul_f32_e32 v58, v68, v42
	v_mul_f32_e32 v59, v69, v43
	global_store_dwordx4 v[54:55], v[28:31], off
	v_mul_f32_e32 v33, v33, v33
	v_fmac_f32_e32 v33, v32, v32
	v_mul_f32_e32 v28, 0x41c00000, v36
	v_mul_f32_e32 v29, 0x41c00000, v37
	v_mul_f32_e32 v30, 0x41c00000, v38
	v_mul_f32_e32 v31, 0x41c00000, v39
	v_mul_f32_e32 v36, 0x41c00000, v48
	v_mul_f32_e32 v37, 0x41c00000, v49
	v_mul_f32_e32 v38, 0x41c00000, v58
	v_mul_f32_e32 v39, 0x41c00000, v59
	v_med3_f32 v28, v28, s51, v177
	v_med3_f32 v29, v29, s51, v177
	v_med3_f32 v30, v30, s51, v177
	v_med3_f32 v31, v31, s51, v177
	v_med3_f32 v36, v36, s51, v177
	v_med3_f32 v37, v37, s51, v177
	v_med3_f32 v38, v38, s51, v177
	v_med3_f32 v39, v39, s51, v177
	v_add_f32_e32 v28, 0x4b400000, v28
	v_add_f32_e32 v29, 0x4b400000, v29
	v_add_f32_e32 v30, 0x4b400000, v30
	v_add_f32_e32 v31, 0x4b400000, v31
	v_add_f32_e32 v36, 0x4b400000, v36
	v_add_f32_e32 v37, 0x4b400000, v37
	v_add_f32_e32 v38, 0x4b400000, v38
	v_add_f32_e32 v39, 0x4b400000, v39
	v_perm_b32 v28, v29, v28, s56
	v_perm_b32 v29, v31, v30, s57
	v_perm_b32 v30, v37, v36, s56
	v_perm_b32 v31, v39, v38, s57
	v_or_b32_e32 v28, v28, v29
	v_or_b32_e32 v29, v30, v31
	global_store_dwordx2 v[26:27], v[28:29], off
	global_load_dwordx4 v[28:31], v[46:47], off offset:512 nt
	s_nop 0
	global_load_dwordx4 v[36:39], v[46:47], off offset:528 nt
	v_mul_f32_e32 v46, v57, v57
	v_fmac_f32_e32 v46, v56, v56
	v_mul_f32_e32 v41, v41, v41
	v_add_f32_e32 v32, v46, v33
	v_fmac_f32_e32 v41, v40, v40
	v_mul_f32_e32 v43, v43, v43
	v_fmac_f32_e32 v43, v42, v42
	v_add_f32_e32 v32, v32, v41
	v_add_f32_e32 v32, v43, v32
	s_waitcnt vmcnt(1)
	v_pk_fma_f32 v[24:25], v[24:25], s[26:27], v[30:31] op_sel_hi:[1,0,1]
	v_pk_fma_f32 v[22:23], v[22:23], s[26:27], v[28:29] op_sel_hi:[1,0,1]
	s_waitcnt vmcnt(0)
	v_pk_fma_f32 v[30:31], v[18:19], s[26:27], v[36:37] op_sel_hi:[1,0,1]
	v_mul_f32_e32 v33, v23, v23
	v_mul_f32_e32 v36, v25, v25
	v_pk_fma_f32 v[28:29], v[20:21], s[26:27], v[38:39] op_sel_hi:[1,0,1]
	v_mul_f32_e32 v37, v31, v31
	v_cvt_pk_bf16_f32 v18, v22, v23
	v_cvt_pk_bf16_f32 v19, v24, v25
	v_cvt_pk_bf16_f32 v20, v30, v31
	v_cvt_pk_bf16_f32 v21, v28, v29
	v_mul_f32_e32 v39, v62, v22
	v_mul_f32_e32 v23, v63, v23
	v_mul_f32_e32 v40, v64, v24
	v_mul_f32_e32 v25, v65, v25
	v_fmac_f32_e32 v33, v22, v22
	v_fmac_f32_e32 v36, v24, v24
	v_mul_f32_e32 v38, v29, v29
	v_fmac_f32_e32 v37, v30, v30
	global_store_dwordx4 v[44:45], v[18:21], off
	v_fmac_f32_e32 v38, v28, v28
	v_mul_f32_e32 v41, v50, v30
	v_mul_f32_e32 v18, 0x41c00000, v39
	v_mul_f32_e32 v19, 0x41c00000, v23
	v_mul_f32_e32 v20, 0x41c00000, v40
	v_mul_f32_e32 v21, 0x41c00000, v25
	v_add_f32_e32 v25, v33, v36
	v_med3_f32 v18, v18, s51, v177
	v_med3_f32 v19, v19, s51, v177
	v_med3_f32 v20, v20, s51, v177
	v_med3_f32 v21, v21, s51, v177
	v_add_f32_e32 v25, v25, v37
	v_add_f32_e32 v18, 0x4b400000, v18
	v_add_f32_e32 v19, 0x4b400000, v19
	v_add_f32_e32 v20, 0x4b400000, v20
	v_add_f32_e32 v21, 0x4b400000, v21
	v_add_f32_e32 v25, v38, v25
	v_perm_b32 v18, v19, v18, s56
	v_perm_b32 v19, v21, v20, s57
	v_add_f32_e32 v21, v32, v25
	v_or_b32_e32 v20, v18, v19
	ds_bpermute_b32 v18, v132, v21
	v_mul_f32_e32 v19, v53, v29
	v_mul_f32_e32 v19, 0x41c00000, v19
	v_mul_f32_e32 v31, v51, v31
	v_mul_f32_e32 v42, v52, v28
	v_med3_f32 v19, v19, s51, v177
	s_waitcnt lgkmcnt(0)
	v_add_f32_e32 v18, v21, v18
	v_mul_f32_e32 v22, 0x41c00000, v41
	v_mul_f32_e32 v23, 0x41c00000, v31
	v_mul_f32_e32 v24, 0x41c00000, v42
	v_add_f32_e32 v25, 0x4b400000, v19
	ds_bpermute_b32 v19, v133, v18
	v_med3_f32 v22, v22, s51, v177
	v_med3_f32 v23, v23, s51, v177
	v_med3_f32 v24, v24, s51, v177
	v_add_f32_e32 v22, 0x4b400000, v22
	v_add_f32_e32 v23, 0x4b400000, v23
	v_add_f32_e32 v24, 0x4b400000, v24
	v_perm_b32 v21, v23, v22, s56
	v_perm_b32 v22, v25, v24, s57
	v_or_b32_e32 v21, v21, v22
	global_store_dwordx2 v[26:27], v[20:21], off offset:128
	s_and_saveexec_b64 s[28:29], s[0:1]
	s_cbranch_execz .LBB0_631
	v_lshlrev_b64 v[20:21], 8, v[34:35]
	v_lshl_add_u64 v[20:21], s[22:23], 0, v[20:21]
	s_waitcnt lgkmcnt(0)
	v_add_f32_e32 v18, v18, v19
	global_store_dword v[20:21], v18, off
; __device__ __forceinline__ unsigned cvt_pk_bf16(float lo, float hi) { unsigned r; asm volatile("v_cvt_pk_bf16_f32 %0, %1, %2" : "=v"(r) : "v"(lo), "v"(hi)); return r; }
; __device__ __forceinline__ unsigned q8x4(const f32x4 a, const f32x4 g, float s) {
;     unsigned y[4];
; #pragma unroll
;     for (int i = 0; i < 4; ++i) y[i] = __float_as_uint(__builtin_fmaf(__builtin_amdgcn_fmed3f(a[i] * g[i] * s, -127.0f, 127.0f), 1.0f, 12582912.0f));
;     return __builtin_amdgcn_perm(y[1], y[0], 0x0c0c0400u) | __builtin_amdgcn_perm(y[3], y[2], 0x04000c0cu);
; }
;     __device__ __forceinline__ void operator()(const f32x4 (&acc)[2][2][4][2], const Unit& u, int wr, int wc, int fr, int fq) const {
;     ...
;             for (int m = 0; m < 4; ++m) { const size_t r = (size_t)(row0 + ai * HALF + m * 16); float ss = 0.f;
; #pragma unroll
;                 for (int bj = 0; bj < 2; ++bj) { const size_t off = r * 4096 + col0 + bj * HALF;
;                     const f32x4 v0 = acc[ai][bj][m][0] * scale + *(const f32x4*)(R + off), v1 = acc[ai][bj][m][1] * scale + *(const f32x4*)(R + off + 4);
;                     ss += (v0[0] * v0[0] + v0[1] * v0[1]) + (v0[2] * v0[2] + v0[3] * v0[3]) + (v1[0] * v1[0] + v1[1] * v1[1]) + (v1[2] * v1[2] + v1[3] * v1[3]);
;                     u32x4 w; w.x = cvt_pk_bf16(v0[0], v0[1]); w.y = cvt_pk_bf16(v0[2], v0[3]); w.z = cvt_pk_bf16(v1[0], v1[1]); w.w = cvt_pk_bf16(v1[2], v1[3]);
;                     *(u32x4*)(HB + off) = w;
;                     u32x2e q; q.x = q8x4(v0, gv[bj][0], (float)HQS); q.y = q8x4(v1, gv[bj][1], (float)HQS);
;                     *(u32x2e*)(Q8 + r * LDQ8 + col0 + bj * HALF) = q; }
;                 ss += __shfl_xor(ss, 16); ss += __shfl_xor(ss, 32);
;                 if (fq == 0) SSQP[r * 64 + u.pn * 4 + wc] = ss; }
.LBB0_631:
	s_or_b64 exec, exec, s[28:29]
	v_add_u32_e32 v18, 0xb0, v140
	s_waitcnt lgkmcnt(0)
	v_ashrrev_i32_e32 v19, 31, v18
	v_lshlrev_b64 v[20:21], 12, v[18:19]
	v_lshl_add_u64 v[28:29], v[20:21], 0, v[138:139]
	v_lshl_add_u64 v[30:31], v[28:29], 2, s[8:9]
	global_load_dwordx4 v[20:23], v[30:31], off nt
	global_load_dwordx4 v[24:27], v[30:31], off offset:16 nt
	v_cvt_f32_i32_e32 v15, v15
	v_cvt_f32_i32_e32 v14, v14
	v_cvt_f32_i32_e32 v17, v17
	v_cvt_f32_i32_e32 v16, v16
	v_cvt_f32_i32_e32 v33, v11
	v_cvt_f32_i32_e32 v32, v10
	v_cvt_f32_i32_e32 v13, v13
	v_cvt_f32_i32_e32 v12, v12
	v_lshlrev_b64 v[28:29], 1, v[28:29]
	v_lshl_add_u64 v[34:35], s[14:15], 0, v[28:29]
	v_mad_i64_i32 v[10:11], s[28:29], v18, s50, v[142:143]
	v_cvt_f32_i32_e32 v7, v7
	v_cvt_f32_i32_e32 v6, v6
	v_cvt_f32_i32_e32 v9, v9
	v_cvt_f32_i32_e32 v8, v8
	v_cvt_f32_i32_e32 v3, v3
	v_cvt_f32_i32_e32 v2, v2
	v_cvt_f32_i32_e32 v5, v5
	v_cvt_f32_i32_e32 v4, v4
	v_or_b32_e32 v28, 0x100, v28
	v_lshl_add_u64 v[28:29], s[14:15], 0, v[28:29]
	s_waitcnt vmcnt(1)
	v_pk_fma_f32 v[16:17], v[16:17], s[26:27], v[22:23] op_sel_hi:[1,0,1]
	v_pk_fma_f32 v[36:37], v[14:15], s[26:27], v[20:21] op_sel_hi:[1,0,1]
	s_waitcnt vmcnt(0)
	v_pk_fma_f32 v[26:27], v[12:13], s[26:27], v[26:27] op_sel_hi:[1,0,1]
	v_pk_fma_f32 v[24:25], v[32:33], s[26:27], v[24:25] op_sel_hi:[1,0,1]
	v_cvt_pk_bf16_f32 v12, v36, v37
	v_cvt_pk_bf16_f32 v13, v16, v17
	v_mul_f32_e32 v20, v74, v36
	v_cvt_pk_bf16_f32 v14, v24, v25
	v_cvt_pk_bf16_f32 v15, v26, v27
	v_mul_f32_e32 v21, v75, v37
	v_mul_f32_e32 v22, v76, v16
	v_mul_f32_e32 v23, v77, v17
	v_mul_f32_e32 v32, v66, v24
	v_mul_f32_e32 v33, v67, v25
	v_mul_f32_e32 v38, v68, v26
	v_mul_f32_e32 v39, v69, v27
	global_store_dwordx4 v[34:35], v[12:15], off
	v_mul_f32_e32 v17, v17, v17
	v_fmac_f32_e32 v17, v16, v16
	v_mul_f32_e32 v12, 0x41c00000, v20
	v_mul_f32_e32 v13, 0x41c00000, v21
	v_mul_f32_e32 v14, 0x41c00000, v22
	v_mul_f32_e32 v15, 0x41c00000, v23
	v_mul_f32_e32 v20, 0x41c00000, v32
	v_mul_f32_e32 v21, 0x41c00000, v33
	v_mul_f32_e32 v22, 0x41c00000, v38
	v_mul_f32_e32 v23, 0x41c00000, v39
	v_med3_f32 v12, v12, s51, v177
	v_med3_f32 v13, v13, s51, v177
	v_med3_f32 v14, v14, s51, v177
	v_med3_f32 v15, v15, s51, v177
	v_med3_f32 v20, v20, s51, v177
	v_med3_f32 v21, v21, s51, v177
	v_med3_f32 v22, v22, s51, v177
	v_med3_f32 v23, v23, s51, v177
	v_add_f32_e32 v12, 0x4b400000, v12
	v_add_f32_e32 v13, 0x4b400000, v13
	v_add_f32_e32 v14, 0x4b400000, v14
	v_add_f32_e32 v15, 0x4b400000, v15
	v_add_f32_e32 v20, 0x4b400000, v20
	v_add_f32_e32 v21, 0x4b400000, v21
	v_add_f32_e32 v22, 0x4b400000, v22
	v_add_f32_e32 v23, 0x4b400000, v23
	v_perm_b32 v12, v13, v12, s56
	v_perm_b32 v13, v15, v14, s57
	v_perm_b32 v14, v21, v20, s56
	v_perm_b32 v15, v23, v22, s57
	v_or_b32_e32 v12, v12, v13
	v_or_b32_e32 v13, v14, v15
	global_store_dwordx2 v[10:11], v[12:13], off
	global_load_dwordx4 v[12:15], v[30:31], off offset:512 nt
	s_nop 0
	global_load_dwordx4 v[20:23], v[30:31], off offset:528 nt
	v_mul_f32_e32 v30, v37, v37
	v_fmac_f32_e32 v30, v36, v36
	v_mul_f32_e32 v25, v25, v25
	v_add_f32_e32 v16, v30, v17
	v_fmac_f32_e32 v25, v24, v24
	v_mul_f32_e32 v27, v27, v27
	v_fmac_f32_e32 v27, v26, v26
	v_add_f32_e32 v16, v16, v25
	v_add_f32_e32 v16, v27, v16
	s_waitcnt vmcnt(1)
	v_pk_fma_f32 v[8:9], v[8:9], s[26:27], v[14:15] op_sel_hi:[1,0,1]
	v_pk_fma_f32 v[6:7], v[6:7], s[26:27], v[12:13] op_sel_hi:[1,0,1]
	s_waitcnt vmcnt(0)
	v_pk_fma_f32 v[14:15], v[2:3], s[26:27], v[20:21] op_sel_hi:[1,0,1]
	v_mul_f32_e32 v17, v7, v7
	v_mul_f32_e32 v20, v9, v9
	v_pk_fma_f32 v[12:13], v[4:5], s[26:27], v[22:23] op_sel_hi:[1,0,1]
	v_mul_f32_e32 v21, v15, v15
	v_cvt_pk_bf16_f32 v2, v6, v7
	v_cvt_pk_bf16_f32 v3, v8, v9
	v_cvt_pk_bf16_f32 v4, v14, v15
	v_cvt_pk_bf16_f32 v5, v12, v13
	v_mul_f32_e32 v23, v62, v6
	v_mul_f32_e32 v7, v63, v7
	v_mul_f32_e32 v24, v64, v8
	v_mul_f32_e32 v9, v65, v9
	v_fmac_f32_e32 v17, v6, v6
	v_fmac_f32_e32 v20, v8, v8
	v_mul_f32_e32 v22, v13, v13
	v_fmac_f32_e32 v21, v14, v14
	global_store_dwordx4 v[28:29], v[2:5], off
	v_fmac_f32_e32 v22, v12, v12
	v_mul_f32_e32 v25, v50, v14
	v_mul_f32_e32 v2, 0x41c00000, v23
	v_mul_f32_e32 v3, 0x41c00000, v7
	v_mul_f32_e32 v4, 0x41c00000, v24
	v_mul_f32_e32 v5, 0x41c00000, v9
	v_add_f32_e32 v9, v17, v20
	v_med3_f32 v2, v2, s51, v177
	v_med3_f32 v3, v3, s51, v177
	v_med3_f32 v4, v4, s51, v177
	v_med3_f32 v5, v5, s51, v177
	v_add_f32_e32 v9, v9, v21
	v_add_f32_e32 v2, 0x4b400000, v2
	v_add_f32_e32 v3, 0x4b400000, v3
	v_add_f32_e32 v4, 0x4b400000, v4
	v_add_f32_e32 v5, 0x4b400000, v5
	v_add_f32_e32 v9, v22, v9
	v_perm_b32 v2, v3, v2, s56
	v_perm_b32 v3, v5, v4, s57
	v_add_f32_e32 v5, v16, v9
	v_or_b32_e32 v4, v2, v3
	ds_bpermute_b32 v2, v132, v5
	v_mul_f32_e32 v3, v53, v13
	v_mul_f32_e32 v3, 0x41c00000, v3
	v_mul_f32_e32 v15, v51, v15
	v_mul_f32_e32 v26, v52, v12
	v_med3_f32 v3, v3, s51, v177
	s_waitcnt lgkmcnt(0)
	v_add_f32_e32 v2, v5, v2
	v_mul_f32_e32 v6, 0x41c00000, v25
	v_mul_f32_e32 v7, 0x41c00000, v15
	v_mul_f32_e32 v8, 0x41c00000, v26
	v_add_f32_e32 v9, 0x4b400000, v3
	ds_bpermute_b32 v3, v133, v2
	v_med3_f32 v6, v6, s51, v177
	v_med3_f32 v7, v7, s51, v177
	v_med3_f32 v8, v8, s51, v177
	v_add_f32_e32 v6, 0x4b400000, v6
	v_add_f32_e32 v7, 0x4b400000, v7
	v_add_f32_e32 v8, 0x4b400000, v8
	v_perm_b32 v5, v7, v6, s56
	v_perm_b32 v6, v9, v8, s57
	v_or_b32_e32 v5, v5, v6
	global_store_dwordx2 v[10:11], v[4:5], off offset:128
	s_and_saveexec_b64 s[28:29], s[0:1]
	s_cbranch_execz .LBB0_633
	v_lshlrev_b64 v[4:5], 8, v[18:19]
	v_lshl_add_u64 v[4:5], s[22:23], 0, v[4:5]
	s_waitcnt lgkmcnt(0)
	v_add_f32_e32 v2, v2, v3
	global_store_dword v[4:5], v2, off
